# MoE-down bias row staged into LDS by wave 0 with one LDS-DMA ahead of the K-loop (double buffered), epilogue reads it with ds_read_b128; on top of the C=0 first-iteration MFMAs
# speedup vs baseline: 1.0017x; 1.0017x over previous
.LBB0_1304:
	s_or_b64 exec, exec, s[2:3]
	s_mov_b32 s85, 0
	s_mov_b64 s[0:1], s[96:97]
	s_mov_b32 s2, s70
	s_mov_b32 s3, -1
	s_waitcnt lgkmcnt(0)
	s_barrier
	s_mov_b32 s16, s73
	v_mbcnt_lo_u32_b32 v0, s3, 0
	v_mbcnt_hi_u32_b32 v0, s3, v0
	v_lshl_add_u32 v2, s2, 6, v0
	s_load_dwordx2 s[6:7], s[0:1], 0xe8
	s_mov_b32 s0, s91
	s_mov_b32 s1, s88
	s_add_i32 s4, s16, 0x20000
	v_cmp_gt_i32_e64 s[2:3], 32, v2
	v_ashrrev_i32_e32 v3, 31, v2
	v_lshl_add_u32 v0, v2, 2, s4
	s_and_saveexec_b64 s[4:5], s[2:3]
	s_cbranch_execz .LBB0_1306
	s_mov_b32 s15, s73
	s_lshl_b64 s[8:9], s[14:15], 2
	s_waitcnt lgkmcnt(0)
	s_add_u32 s8, s6, s8
	s_addc_u32 s9, s7, s9
	v_lshl_add_u64 v[4:5], v[2:3], 2, s[8:9]
	v_add_co_u32_e32 v4, vcc, 0x10000, v4
	s_nop 1
	v_addc_co_u32_e32 v5, vcc, 0, v5, vcc
	global_load_dword v4, v[4:5], off sc1
	s_waitcnt vmcnt(0)
	ds_write_b32 v0, v4 offset:128

.LBB0_1348:
	s_ashr_i32 s15, s14, 31
	s_lshl_b64 s[18:19], s[14:15], 18
	s_add_u32 s18, s40, s18
	s_addc_u32 s19, s41, s19
	s_and_b64 s[20:21], s[2:3], exec
	s_cselect_b32 s15, s19, s29
	s_cselect_b32 s64, s18, s28
	s_ashr_i32 s17, s16, 31
	s_lshl_b64 s[20:21], s[16:17], 20
	s_add_u32 s17, s42, s20
	s_addc_u32 s30, s43, s21
	s_ashr_i32 s13, s12, 31
	s_lshl_b64 s[20:21], s[12:13], 18
	s_add_u32 s20, s17, s20
	s_addc_u32 s21, s30, s21
	s_and_b64 s[30:31], s[2:3], exec
	s_cselect_b32 s13, s21, s27
	s_cselect_b32 s17, s20, s26
	s_add_u32 s65, s26, 0x100
	s_addc_u32 s66, s27, 0
	s_add_u32 s26, s28, 0x80
	v_mov_b32_e32 v2, 0
	s_addc_u32 s27, s29, 0
	s_mov_b32 s67, -2
	v_mov_b32_e32 v3, v2
	s_waitcnt vmcnt(0)
	s_xor_b32 s85, s85, 0x400
	s_cmp_eq_u32 s70, 0
	s_cbranch_scc0 .Ldb_skip
	s_load_dwordx2 s[98:99], s[96:97], 0xd0
	v_mbcnt_lo_u32_b32 v248, -1, 0
	v_mbcnt_hi_u32_b32 v248, -1, v248
	v_lshlrev_b32_e32 v248, 4, v248
	v_lshl_add_u32 v249, v130, 12, v248
	s_lshl_b32 s92, s24, 10
	v_add_u32_e32 v249, s92, v249
	s_add_i32 m0, s85, 0x26800
	s_waitcnt lgkmcnt(0)
	s_add_u32 s98, s98, s10
	s_addc_u32 s99, s99, s11
	s_nop 0
	global_load_lds_dwordx4 v249, s[98:99]

.LBB0_1352:
	s_mov_b32 s13, -1
	s_mov_b64 s[26:27], s[96:97]
	s_load_dwordx2 s[28:29], s[26:27], 0xd0
	v_mbcnt_lo_u32_b32 v0, s13, 0
	v_mbcnt_hi_u32_b32 v0, s13, v0
	v_lshrrev_b32_e32 v132, 1, v0
	v_ashrrev_i32_e32 v131, 31, v130
	s_waitcnt lgkmcnt(0)
	s_add_u32 s28, s28, s10
	s_addc_u32 s29, s29, s11
	s_lshl_b32 s13, s24, 8
	v_and_or_b32 v132, v132, 24, s13
	v_lshlrev_b64 v[130:131], 12, v[130:131]
	v_or_b32_e32 v138, s53, v132
	v_lshl_add_u64 v[130:131], s[28:29], 0, v[130:131]
	v_ashrrev_i32_e32 v139, 31, v138
	v_lshl_add_u64 v[142:143], v[138:139], 2, v[130:131]
	v_and_b32_e32 v239, 0xff, v138
	v_lshlrev_b32_e32 v239, 2, v239
	v_add_u32_e32 v239, s85, v239
	v_add_u32_e32 v239, 0x26800, v239
	ds_read_b128 v[134:137], v239
	ds_read_b128 v[130:133], v239 offset:16
	s_load_dwordx2 s[26:27], s[26:27], 0xe8
	v_and_or_b32 v0, v0, 15, s52
	v_lshl_add_u32 v172, s22, 8, v0
	v_or_b32_e32 v140, 16, v172
	v_or_b32_e32 v144, 32, v172
	v_add_u32_e32 v158, 0x80, v172
	v_ashrrev_i32_e32 v141, 31, v140
	v_ashrrev_i32_e32 v145, 31, v144
	v_ashrrev_i32_e32 v159, 31, v158
	v_lshlrev_b64 v[162:163], 10, v[140:141]
	v_lshlrev_b64 v[164:165], 10, v[144:145]
	v_lshlrev_b64 v[176:177], 10, v[158:159]
	s_waitcnt lgkmcnt(0)
	v_lshl_add_u64 v[158:159], s[26:27], 0, v[138:139]
	ds_read_b128 v[138:141], v239 offset:528
	ds_read_b128 v[142:145], v239 offset:512
	v_mov_b32_e32 v157, v1
	v_mov_b32_e32 v148, v1
	v_mov_b32_e32 v149, v1
	v_mov_b32_e32 v150, v1
	v_mov_b32_e32 v151, v1
	v_mov_b32_e32 v152, v1
	v_mov_b32_e32 v153, v1
	v_mov_b32_e32 v154, v1
	v_mov_b32_e32 v155, v1
	v_mov_b32_e32 v156, v1
	v_or_b32_e32 v146, 48, v172
	v_add_u32_e32 v174, 0x90, v172
	v_ashrrev_i32_e32 v173, 31, v172
	v_ashrrev_i32_e32 v147, 31, v146
	v_ashrrev_i32_e32 v175, 31, v174
	v_lshlrev_b64 v[160:161], 10, v[172:173]
	v_lshlrev_b64 v[146:147], 10, v[146:147]
	v_lshl_add_u64 v[178:179], v[158:159], 0, s[80:81]
	v_lshl_add_u64 v[160:161], v[178:179], 0, v[160:161]
	v_lshl_add_u64 v[158:159], v[178:179], 0, v[146:147]
	v_lshl_add_u64 v[146:147], v[178:179], 0, v[176:177]
	s_andn2_b64 vcc, exec, s[2:3]
	s_mov_b64 s[2:3], -1
	s_mov_b32 s68, s94
	v_lshl_add_u64 v[162:163], v[178:179], 0, v[162:163]
	v_lshl_add_u64 v[164:165], v[178:179], 0, v[164:165]
	s_waitcnt lgkmcnt(0)
	v_pk_fma_f32 v[86:87], v[86:87], s[86:87], v[134:135] op_sel_hi:[1,0,1]
	v_pk_fma_f32 v[90:91], v[90:91], s[86:87], v[130:131] op_sel_hi:[1,0,1]
	v_pk_fma_f32 v[78:79], v[78:79], s[86:87], v[134:135] op_sel_hi:[1,0,1]
	v_cvt_pk_fp8_f32 v157, v90, v91
	v_mov_b32_e32 v90, v1
	v_cvt_pk_fp8_f32 v90, v86, v87
	v_mov_b32_e32 v86, v1
	v_cvt_pk_fp8_f32 v86, v78, v79
	v_pk_fma_f32 v[58:59], v[58:59], s[86:87], v[130:131] op_sel_hi:[1,0,1]
	v_mov_b32_e32 v79, v1
	v_cvt_pk_fp8_f32 v79, v58, v59
	v_pk_fma_f32 v[66:67], v[66:67], s[86:87], v[134:135] op_sel_hi:[1,0,1]
	v_mov_b32_e32 v78, v1
	v_pk_fma_f32 v[60:61], v[60:61], s[86:87], v[132:133] op_sel_hi:[1,0,1]
	v_cvt_pk_fp8_f32 v78, v66, v67
	v_cvt_pk_fp8_f32 v79, v60, v61 op_sel:[0,0,1]
	v_pk_fma_f32 v[60:61], v[70:71], s[86:87], v[142:143] op_sel_hi:[1,0,1]
	v_mov_b32_e32 v66, v1
	v_cvt_pk_fp8_f32 v66, v60, v61
	v_pk_fma_f32 v[60:61], v[72:73], s[86:87], v[144:145] op_sel_hi:[1,0,1]
	v_pk_fma_f32 v[54:55], v[54:55], s[86:87], v[142:143] op_sel_hi:[1,0,1]
	v_pk_fma_f32 v[50:51], v[50:51], s[86:87], v[138:139] op_sel_hi:[1,0,1]
	v_cvt_pk_fp8_f32 v66, v60, v61 op_sel:[0,0,1]
	v_mov_b32_e32 v60, v1
	v_cvt_pk_fp8_f32 v60, v54, v55
	v_mov_b32_e32 v61, v1
	v_cvt_pk_fp8_f32 v61, v50, v51
	v_pk_fma_f32 v[50:51], v[56:57], s[86:87], v[144:145] op_sel_hi:[1,0,1]
	v_pk_fma_f32 v[46:47], v[46:47], s[86:87], v[142:143] op_sel_hi:[1,0,1]
	v_cvt_pk_fp8_f32 v60, v50, v51 op_sel:[0,0,1]
	v_mov_b32_e32 v50, v1
	v_cvt_pk_fp8_f32 v50, v46, v47
	v_pk_fma_f32 v[42:43], v[42:43], s[86:87], v[138:139] op_sel_hi:[1,0,1]
	v_mov_b32_e32 v51, v1
	v_cvt_pk_fp8_f32 v51, v42, v43
	v_pk_fma_f32 v[42:43], v[48:49], s[86:87], v[144:145] op_sel_hi:[1,0,1]
	v_pk_fma_f32 v[38:39], v[38:39], s[86:87], v[142:143] op_sel_hi:[1,0,1]
	v_cvt_pk_fp8_f32 v50, v42, v43 op_sel:[0,0,1]
	v_mov_b32_e32 v42, v1
	v_cvt_pk_fp8_f32 v42, v38, v39
	v_pk_fma_f32 v[34:35], v[34:35], s[86:87], v[138:139] op_sel_hi:[1,0,1]
	v_mov_b32_e32 v43, v1
	v_cvt_pk_fp8_f32 v43, v34, v35
	v_pk_fma_f32 v[34:35], v[40:41], s[86:87], v[144:145] op_sel_hi:[1,0,1]
	v_pk_fma_f32 v[30:31], v[30:31], s[86:87], v[142:143] op_sel_hi:[1,0,1]
	v_cvt_pk_fp8_f32 v42, v34, v35 op_sel:[0,0,1]
	v_mov_b32_e32 v34, v1
	v_cvt_pk_fp8_f32 v34, v30, v31
	v_pk_fma_f32 v[26:27], v[26:27], s[86:87], v[138:139] op_sel_hi:[1,0,1]
	v_mov_b32_e32 v35, v1
	v_cvt_pk_fp8_f32 v35, v26, v27
	v_pk_fma_f32 v[26:27], v[32:33], s[86:87], v[144:145] op_sel_hi:[1,0,1]
	v_pk_fma_f32 v[22:23], v[22:23], s[86:87], v[142:143] op_sel_hi:[1,0,1]
	v_cvt_pk_fp8_f32 v34, v26, v27 op_sel:[0,0,1]
	v_mov_b32_e32 v26, v1
	v_cvt_pk_fp8_f32 v26, v22, v23
	v_pk_fma_f32 v[18:19], v[18:19], s[86:87], v[138:139] op_sel_hi:[1,0,1]
	v_mov_b32_e32 v27, v1
	v_cvt_pk_fp8_f32 v27, v18, v19
	v_pk_fma_f32 v[18:19], v[24:25], s[86:87], v[144:145] op_sel_hi:[1,0,1]
	v_pk_fma_f32 v[14:15], v[14:15], s[86:87], v[142:143] op_sel_hi:[1,0,1]
	v_cvt_pk_fp8_f32 v26, v18, v19 op_sel:[0,0,1]
	v_mov_b32_e32 v18, v1
	v_cvt_pk_fp8_f32 v18, v14, v15
	v_pk_fma_f32 v[126:127], v[126:127], s[86:87], v[134:135] op_sel_hi:[1,0,1]
	v_pk_fma_f32 v[122:123], v[122:123], s[86:87], v[130:131] op_sel_hi:[1,0,1]
	v_pk_fma_f32 v[82:83], v[82:83], s[86:87], v[130:131] op_sel_hi:[1,0,1]
	v_mov_b32_e32 v91, v1
	v_pk_fma_f32 v[74:75], v[74:75], s[86:87], v[130:131] op_sel_hi:[1,0,1]
	v_mov_b32_e32 v87, v1
	v_pk_fma_f32 v[62:63], v[62:63], s[86:87], v[138:139] op_sel_hi:[1,0,1]
	v_mov_b32_e32 v67, v1
	v_pk_fma_f32 v[118:119], v[118:119], s[86:87], v[134:135] op_sel_hi:[1,0,1]
	v_pk_fma_f32 v[114:115], v[114:115], s[86:87], v[130:131] op_sel_hi:[1,0,1]
	v_cvt_pk_fp8_f32 v148, v126, v127
	v_cvt_pk_fp8_f32 v149, v122, v123
	v_cvt_pk_fp8_f32 v91, v82, v83
	v_cvt_pk_fp8_f32 v87, v74, v75
	v_cvt_pk_fp8_f32 v67, v62, v63
	v_pk_fma_f32 v[10:11], v[10:11], s[86:87], v[138:139] op_sel_hi:[1,0,1]
	v_mov_b32_e32 v19, v1
	v_pk_fma_f32 v[110:111], v[110:111], s[86:87], v[134:135] op_sel_hi:[1,0,1]
	v_pk_fma_f32 v[106:107], v[106:107], s[86:87], v[130:131] op_sel_hi:[1,0,1]
	v_cvt_pk_fp8_f32 v150, v118, v119
	v_cvt_pk_fp8_f32 v151, v114, v115
	v_cvt_pk_fp8_f32 v19, v10, v11
	v_pk_fma_f32 v[10:11], v[16:17], s[86:87], v[144:145] op_sel_hi:[1,0,1]
	v_pk_fma_f32 v[102:103], v[102:103], s[86:87], v[134:135] op_sel_hi:[1,0,1]
	v_pk_fma_f32 v[98:99], v[98:99], s[86:87], v[130:131] op_sel_hi:[1,0,1]
	v_cvt_pk_fp8_f32 v152, v110, v111
	v_cvt_pk_fp8_f32 v153, v106, v107
	v_cvt_pk_fp8_f32 v18, v10, v11 op_sel:[0,0,1]
	v_pk_fma_f32 v[6:7], v[6:7], s[86:87], v[142:143] op_sel_hi:[1,0,1]
	v_pk_fma_f32 v[2:3], v[2:3], s[86:87], v[138:139] op_sel_hi:[1,0,1]
	v_mov_b32_e32 v10, v1
	v_mov_b32_e32 v11, v1
	v_pk_fma_f32 v[128:129], v[128:129], s[86:87], v[136:137] op_sel_hi:[1,0,1]
	v_pk_fma_f32 v[124:125], v[124:125], s[86:87], v[132:133] op_sel_hi:[1,0,1]
	v_pk_fma_f32 v[94:95], v[94:95], s[86:87], v[134:135] op_sel_hi:[1,0,1]
	v_cvt_pk_fp8_f32 v154, v102, v103
	v_cvt_pk_fp8_f32 v155, v98, v99
	v_pk_fma_f32 v[82:83], v[88:89], s[86:87], v[136:137] op_sel_hi:[1,0,1]
	v_pk_fma_f32 v[84:85], v[84:85], s[86:87], v[132:133] op_sel_hi:[1,0,1]
	v_pk_fma_f32 v[74:75], v[80:81], s[86:87], v[136:137] op_sel_hi:[1,0,1]
	v_pk_fma_f32 v[76:77], v[76:77], s[86:87], v[132:133] op_sel_hi:[1,0,1]
	v_pk_fma_f32 v[58:59], v[68:69], s[86:87], v[136:137] op_sel_hi:[1,0,1]
	v_pk_fma_f32 v[62:63], v[64:65], s[86:87], v[140:141] op_sel_hi:[1,0,1]
	v_pk_fma_f32 v[28:29], v[28:29], s[86:87], v[140:141] op_sel_hi:[1,0,1]
	v_cvt_pk_fp8_f32 v10, v6, v7
	v_cvt_pk_fp8_f32 v11, v2, v3
	v_pk_fma_f32 v[120:121], v[120:121], s[86:87], v[136:137] op_sel_hi:[1,0,1]
	v_pk_fma_f32 v[116:117], v[116:117], s[86:87], v[132:133] op_sel_hi:[1,0,1]
	v_cvt_pk_fp8_f32 v156, v94, v95
	v_cvt_pk_fp8_f32 v148, v128, v129 op_sel:[0,0,1]
	v_cvt_pk_fp8_f32 v149, v124, v125 op_sel:[0,0,1]
	v_cvt_pk_fp8_f32 v90, v82, v83 op_sel:[0,0,1]
	v_cvt_pk_fp8_f32 v91, v84, v85 op_sel:[0,0,1]
	v_add_u32_e32 v84, 0xa0, v172
	v_cvt_pk_fp8_f32 v86, v74, v75 op_sel:[0,0,1]
	v_cvt_pk_fp8_f32 v87, v76, v77 op_sel:[0,0,1]
	v_add_u32_e32 v76, 0xb0, v172
	v_cvt_pk_fp8_f32 v78, v58, v59 op_sel:[0,0,1]
	v_cvt_pk_fp8_f32 v67, v62, v63 op_sel:[0,0,1]
	v_pk_fma_f32 v[52:53], v[52:53], s[86:87], v[140:141] op_sel_hi:[1,0,1]
	v_cvt_pk_fp8_f32 v35, v28, v29 op_sel:[0,0,1]
	v_pk_fma_f32 v[20:21], v[20:21], s[86:87], v[140:141] op_sel_hi:[1,0,1]
	v_pk_fma_f32 v[112:113], v[112:113], s[86:87], v[136:137] op_sel_hi:[1,0,1]
	v_pk_fma_f32 v[108:109], v[108:109], s[86:87], v[132:133] op_sel_hi:[1,0,1]
	v_cvt_pk_fp8_f32 v150, v120, v121 op_sel:[0,0,1]
	v_cvt_pk_fp8_f32 v151, v116, v117 op_sel:[0,0,1]
	v_ashrrev_i32_e32 v85, 31, v84
	v_ashrrev_i32_e32 v77, 31, v76
	v_cvt_pk_fp8_f32 v61, v52, v53 op_sel:[0,0,1]
	v_pk_fma_f32 v[44:45], v[44:45], s[86:87], v[140:141] op_sel_hi:[1,0,1]
	v_cvt_pk_fp8_f32 v27, v20, v21 op_sel:[0,0,1]
	v_pk_fma_f32 v[12:13], v[12:13], s[86:87], v[140:141] op_sel_hi:[1,0,1]
	v_pk_fma_f32 v[104:105], v[104:105], s[86:87], v[136:137] op_sel_hi:[1,0,1]
	v_pk_fma_f32 v[100:101], v[100:101], s[86:87], v[132:133] op_sel_hi:[1,0,1]
	v_cvt_pk_fp8_f32 v152, v112, v113 op_sel:[0,0,1]
	v_cvt_pk_fp8_f32 v153, v108, v109 op_sel:[0,0,1]
	v_lshlrev_b64 v[82:83], 10, v[174:175]
	v_lshlrev_b64 v[74:75], 10, v[84:85]
	v_lshlrev_b64 v[58:59], 10, v[76:77]
	v_cvt_pk_fp8_f32 v51, v44, v45 op_sel:[0,0,1]
	v_pk_fma_f32 v[36:37], v[36:37], s[86:87], v[140:141] op_sel_hi:[1,0,1]
	v_cvt_pk_fp8_f32 v19, v12, v13 op_sel:[0,0,1]
	v_pk_fma_f32 v[2:3], v[8:9], s[86:87], v[144:145] op_sel_hi:[1,0,1]
	v_pk_fma_f32 v[4:5], v[4:5], s[86:87], v[140:141] op_sel_hi:[1,0,1]
	v_pk_fma_f32 v[96:97], v[96:97], s[86:87], v[136:137] op_sel_hi:[1,0,1]
	v_pk_fma_f32 v[92:93], v[92:93], s[86:87], v[132:133] op_sel_hi:[1,0,1]
	v_cvt_pk_fp8_f32 v154, v104, v105 op_sel:[0,0,1]
	v_cvt_pk_fp8_f32 v155, v100, v101 op_sel:[0,0,1]
	v_lshl_add_u64 v[82:83], v[178:179], 0, v[82:83]
	v_lshl_add_u64 v[74:75], v[178:179], 0, v[74:75]
	v_lshl_add_u64 v[58:59], v[178:179], 0, v[58:59]
	v_cvt_pk_fp8_f32 v43, v36, v37 op_sel:[0,0,1]
	v_cvt_pk_fp8_f32 v10, v2, v3 op_sel:[0,0,1]
	v_cvt_pk_fp8_f32 v11, v4, v5 op_sel:[0,0,1]
	v_cvt_pk_fp8_f32 v156, v96, v97 op_sel:[0,0,1]
	v_cvt_pk_fp8_f32 v157, v92, v93 op_sel:[0,0,1]
	s_mov_b32 s98, -1
	v_mbcnt_lo_u32_b32 v180, s98, 0
	v_mbcnt_hi_u32_b32 v180, s98, v180
	v_and_b32_e32 v181, 3, v180
	v_lshrrev_b32_e32 v182, 2, v180
	v_lshlrev_b32_e32 v183, 4, v181
	v_or_b32_e32 v183, v183, v182
	v_lshlrev_b32_e32 v183, 2, v183
	ds_bpermute_b32 v148, v183, v148
	ds_bpermute_b32 v149, v183, v149
	ds_bpermute_b32 v150, v183, v150
	ds_bpermute_b32 v151, v183, v151
	ds_bpermute_b32 v152, v183, v152
	ds_bpermute_b32 v153, v183, v153
	ds_bpermute_b32 v154, v183, v154
	ds_bpermute_b32 v155, v183, v155
	ds_bpermute_b32 v156, v183, v156
	ds_bpermute_b32 v157, v183, v157
	ds_bpermute_b32 v90, v183, v90
	ds_bpermute_b32 v91, v183, v91
	ds_bpermute_b32 v86, v183, v86
	ds_bpermute_b32 v87, v183, v87
	ds_bpermute_b32 v78, v183, v78
	ds_bpermute_b32 v79, v183, v79
	ds_bpermute_b32 v66, v183, v66
	ds_bpermute_b32 v67, v183, v67
	ds_bpermute_b32 v60, v183, v60
	ds_bpermute_b32 v61, v183, v61
	ds_bpermute_b32 v50, v183, v50
	ds_bpermute_b32 v51, v183, v51
	ds_bpermute_b32 v42, v183, v42
	ds_bpermute_b32 v43, v183, v43
	ds_bpermute_b32 v34, v183, v34
	ds_bpermute_b32 v35, v183, v35
	ds_bpermute_b32 v26, v183, v26
	ds_bpermute_b32 v27, v183, v27
	ds_bpermute_b32 v18, v183, v18
	ds_bpermute_b32 v19, v183, v19
	ds_bpermute_b32 v10, v183, v10
	ds_bpermute_b32 v11, v183, v11
	v_lshlrev_b32_e32 v184, 3, v181
	v_or_b32_e32 v184, s13, v184
	v_or_b32_e32 v184, s53, v184
	v_mov_b32_e32 v185, 0
	v_lshl_add_u64 v[184:185], s[26:27], 0, v[184:185]
	v_lshl_add_u64 v[184:185], v[184:185], 0, s[80:81]
	v_or_b32_e32 v186, s52, v182
	v_lshl_add_u32 v186, s22, 8, v186
	v_lshlrev_b32_e32 v186, 10, v186
	v_mov_b32_e32 v187, 0
	v_lshl_add_u64 v[186:187], v[184:185], 0, v[186:187]
	s_mov_b32 s99, 0
	s_mov_b32 s98, 0x0
	v_lshl_add_u64 v[190:191], v[186:187], 0, s[98:99]
	s_mov_b32 s98, 0x4000
	v_lshl_add_u64 v[192:193], v[186:187], 0, s[98:99]
	s_mov_b32 s98, 0x8000
	v_lshl_add_u64 v[194:195], v[186:187], 0, s[98:99]
	s_mov_b32 s98, 0xc000
	v_lshl_add_u64 v[196:197], v[186:187], 0, s[98:99]
	s_mov_b32 s98, 0x20000
	v_lshl_add_u64 v[198:199], v[186:187], 0, s[98:99]
	s_mov_b32 s98, 0x24000
	v_lshl_add_u64 v[200:201], v[186:187], 0, s[98:99]
	s_mov_b32 s98, 0x28000
	v_lshl_add_u64 v[202:203], v[186:187], 0, s[98:99]
	s_mov_b32 s98, 0x2c000
	v_lshl_add_u64 v[204:205], v[186:187], 0, s[98:99]
	s_waitcnt lgkmcnt(0)
	global_store_dwordx2 v[190:191], v[148:149], off
	global_store_dwordx2 v[192:193], v[150:151], off
	global_store_dwordx2 v[194:195], v[152:153], off
	global_store_dwordx2 v[196:197], v[154:155], off
	global_store_dwordx2 v[198:199], v[156:157], off
	global_store_dwordx2 v[200:201], v[90:91], off
	global_store_dwordx2 v[202:203], v[86:87], off
	global_store_dwordx2 v[204:205], v[78:79], off
	global_store_dwordx2 v[190:191], v[66:67], off offset:128
	global_store_dwordx2 v[192:193], v[60:61], off offset:128
	global_store_dwordx2 v[194:195], v[50:51], off offset:128
	global_store_dwordx2 v[196:197], v[42:43], off offset:128
	global_store_dwordx2 v[198:199], v[34:35], off offset:128
	global_store_dwordx2 v[200:201], v[26:27], off offset:128
	global_store_dwordx2 v[202:203], v[18:19], off offset:128
	global_store_dwordx2 v[204:205], v[10:11], off offset:128
	s_cbranch_vccnz .LBB0_1341
	s_andn2_b64 vcc, exec, s[6:7]
	s_cbranch_vccnz .LBB0_1340
	s_barrier
	s_branch .LBB0_1340
